# MLA tile loop: K/V ring slot folded into LDS read immediate offsets (one copy of QK and softmax+PV code per slot), accumulator init with 64-bit moves
# baseline (speedup 1.0000x reference)
; template <int DQ>
; DI AtRd at_rd_init(int lane) {
;     AtRd r; const int kr = lane & 31, h = lane >> 5, i16 = lane & 15, q = i16 >> 2, pp = i16 & 3, blk = (lane >> 4) & 1;
;     const int f = at_kf<DQ>(kr);
;     r.kbase = kr * (DQ * 2) + ((f >> 3) << 7); r.kbase1 = kr * (DQ * 2) + (((f >> 3) ^ 1) << 7);
; #pragma unroll
;     for (int i = 0; i < 4; ++i) r.ko[i] = ((2 * i + h) ^ (f & 7)) << 4;
;     r.vbase = (4 * h + q) * 256 + 8 * pp;
; #pragma unroll
;     for (int t = 0; t < 4; ++t) r.vo[t] = ((2 * t + blk) ^ ((4 * h + q) & 7)) << 5;
;     return r;
; template <int DQ>
; DI AtDma at_dma_init(int ld_bytes, int wave, int lane) {
;     AtDma d; d.rope = 0u;
;     constexpr int PPR = DQ / 8;
; #pragma unroll
;     for (int k = 0; k < DQ / 64; ++k) { const int L = (wave + 8 * k) * 64 + lane, r = L / PPR, pc = (L % PPR) ^ at_kf<DQ>(r);
;         if (DQ == 192 && pc >= 16) { d.ko[k] = (unsigned)(r * 128 + (pc - 16) * 16); d.rope |= 1u << k; } else d.ko[k] = (unsigned)(r * ld_bytes + pc * 16); }
;     if (DQ == 128) d.ko[2] = 0u;
; #pragma unroll
;     for (int k = 0; k < 2; ++k) { const int L = (wave + 8 * k) * 64 + lane, r = L >> 4, pc = (L & 15) ^ (2 * (r & 7)); d.vo[k] = (unsigned)(r * ld_bytes + pc * 16); }
;     return d;
; }
.LBB0_530:
	s_cmp_gt_i32 s24, 5
	s_cselect_b64 s[0:1], -1, 0
	s_cmp_lt_i32 s25, 6
	s_cselect_b64 s[2:3], -1, 0
	s_or_b64 s[0:1], s[0:1], s[2:3]
	s_and_b64 vcc, exec, s[0:1]
	s_cbranch_vccnz .LBB0_622
	s_bitcmp1_b32 s26, 1
	s_cbranch_scc1 .LBB0_560
	v_readfirstlane_b32 s2, v0
	s_movk_i32 s0, 0xffc0
	s_nop 0
	v_mov_b32_e32 v1, s2
	v_bfi_b32 v2, s0, v1, v0
	s_mov_b32 s0, 0x2aaaaaab
	v_mul_hi_i32 v1, v2, s0
	v_lshrrev_b32_e32 v3, 31, v1
	v_ashrrev_i32_e32 v1, 2, v1
	v_add_u32_e32 v1, v1, v3
	v_mul_lo_u32 v3, v1, 24
	v_sub_u32_e32 v3, v2, v3
	v_lshrrev_b32_e32 v4, 1, v1
	v_bitop3_b32 v3, v4, v3, 7 bitop3:0x6c
	v_cmp_gt_i32_e32 vcc, 16, v3
	v_lshlrev_b32_e32 v3, 4, v3
	s_and_saveexec_b64 s[0:1], vcc
	s_xor_b64 s[0:1], exec, s[0:1]
	v_lshl_add_u32 v162, v1, 12, v3
	s_or_saveexec_b64 s[0:1], s[0:1]
	v_mov_b32_e32 v4, 0
	s_xor_b64 exec, exec, s[0:1]
	v_lshlrev_b32_e32 v1, 7, v1
	s_movk_i32 s3, 0xff00
	v_add3_u32 v162, v1, v3, s3
	v_mov_b32_e32 v4, 1
	s_or_b64 exec, exec, s[0:1]
	v_add_u32_e32 v5, 0x200, v2
	s_mov_b32 s0, 0x2aaaaaab
	v_mul_hi_i32 v1, v5, s0
	v_lshrrev_b32_e32 v3, 31, v1
	v_ashrrev_i32_e32 v1, 2, v1
	v_add_u32_e32 v1, v1, v3
	v_mul_lo_u32 v3, v1, 24
	v_sub_u32_e32 v3, v5, v3
	v_lshrrev_b32_e32 v6, 1, v1
	v_bitop3_b32 v3, v6, v3, 7 bitop3:0x6c
	v_cmp_gt_i32_e32 vcc, 16, v3
	v_lshlrev_b32_e32 v3, 4, v3
	s_and_saveexec_b64 s[0:1], vcc
	s_xor_b64 s[0:1], exec, s[0:1]
	v_lshl_add_u32 v164, v1, 12, v3
	s_andn2_saveexec_b64 s[0:1], s[0:1]
	v_lshlrev_b32_e32 v1, 7, v1
	s_movk_i32 s3, 0xff00
	v_add3_u32 v164, v1, v3, s3
	v_or_b32_e32 v4, 2, v4
	s_or_b64 exec, exec, s[0:1]
	v_add_u32_e32 v3, 0x400, v2
	s_mov_b32 s0, 0x2aaaaaab
	v_mul_hi_i32 v1, v3, s0
	v_lshrrev_b32_e32 v6, 31, v1
	v_ashrrev_i32_e32 v1, 2, v1
	v_add_u32_e32 v1, v1, v6
	v_mul_lo_u32 v6, v1, 24
	v_sub_u32_e32 v3, v3, v6
	v_lshrrev_b32_e32 v6, 1, v1
	v_bitop3_b32 v3, v6, v3, 7 bitop3:0x6c
	v_cmp_gt_i32_e32 vcc, 16, v3
	v_lshlrev_b32_e32 v6, 4, v3
	s_and_saveexec_b64 s[0:1], vcc
	s_xor_b64 s[0:1], exec, s[0:1]
	v_lshl_add_u32 v166, v1, 12, v6
	s_or_saveexec_b64 s[0:1], s[0:1]
	v_and_b32_e32 v3, 63, v0
	s_xor_b64 exec, exec, s[0:1]
	v_lshlrev_b32_e32 v1, 7, v1
	s_movk_i32 s3, 0xff00
	v_add3_u32 v166, v1, v6, s3
	v_or_b32_e32 v4, 4, v4
	s_or_b64 exec, exec, s[0:1]
	v_lshrrev_b32_e32 v6, 5, v3
	v_bfe_u32 v10, v0, 1, 3
	s_lshr_b32 s2, s2, 6
	v_bitop3_b32 v11, v6, v10, 2 bitop3:0x36
	s_add_u32 s0, s50, 0x2c5ae000
	v_lshrrev_b32_e32 v1, 1, v0
	v_lshlrev_b32_e32 v180, 4, v11
	v_bitop3_b32 v11, v6, v10, 4 bitop3:0x36
	v_bitop3_b32 v10, v6, v10, 6 bitop3:0x36
	s_addc_u32 s1, s51, 0
	v_bitop3_b32 v1, v6, v1, 7 bitop3:0x78
	v_lshlrev_b32_e32 v182, 4, v10
	v_bfe_u32 v10, v3, 2, 2
	v_lshlrev_b32_e32 v6, 2, v6
	s_add_u32 s8, s50, 0x304ae000
	v_lshrrev_b32_e32 v8, 2, v3
	v_lshrrev_b32_e32 v9, 4, v3
	v_lshlrev_b32_e32 v181, 4, v11
	v_bfe_u32 v3, v3, 4, 1
	v_or_b32_e32 v11, v6, v10
	s_addc_u32 s9, s51, 0
	v_bitop3_b32 v14, v6, v3, v10 bitop3:0x36
	v_bitop3_b32 v3, v3, v11, 4 bitop3:0x36
	s_lshr_b32 s4, s23, 31
	v_and_b32_e32 v7, 31, v0
	v_lshlrev_b32_e32 v183, 5, v14
	v_or_b32_e32 v14, 2, v9
	v_lshlrev_b32_e32 v185, 5, v3
	v_or_b32_e32 v3, 6, v9
	s_movk_i32 s3, 0x180
	s_add_i32 s4, s23, s4
	v_ashrrev_i32_e32 v2, 4, v2
	v_bitop3_b32 v14, v6, v14, v10 bitop3:0x36
	v_bitop3_b32 v3, v6, v3, v10 bitop3:0x36
	v_and_b32_e32 v9, 15, v0
	v_mad_u32_u24 v187, v7, s3, 0
	s_add_i32 s3, s23, s22
	s_ashr_i32 s4, s4, 1
	v_lshlrev_b32_e32 v10, 1, v2
	s_sub_i32 s10, s3, s4
	v_bitop3_b32 v10, v10, v9, 14 bitop3:0x6c
	v_lshlrev_b32_e32 v2, 12, v2
	s_add_u32 s12, s50, 0x2e0ae000
	v_lshl_or_b32 v168, v10, 4, v2
	v_ashrrev_i32_e32 v2, 4, v5
	s_addc_u32 s13, s51, 0
	v_lshlrev_b32_e32 v5, 1, v2
	s_add_u32 s14, s50, 0x2c48e000
	v_bitop3_b32 v5, v5, v9, 14 bitop3:0x6c
	v_lshlrev_b32_e32 v2, 12, v2
	s_addc_u32 s15, s51, 0
	v_lshl_or_b32 v170, v5, 4, v2
	v_lshl_or_b32 v189, s2, 5, v7
	s_lshl_b32 s2, s2, 10
	v_and_b32_e32 v2, 1, v4
	s_add_i32 s27, s2, 0
	v_cmp_eq_u32_e64 s[2:3], 0, v2
	v_and_b32_e32 v2, 2, v4
	s_abs_i32 s16, s23
	v_cmp_eq_u32_e64 s[4:5], 0, v2
	v_cvt_f32_u32_e32 v2, s16
	s_sub_i32 s18, 0, s16
	s_ashr_i32 s17, s10, 31
	s_abs_i32 s10, s10
	v_rcp_iflag_f32_e32 v2, v2
	v_lshlrev_b32_e32 v13, 3, v0
	v_lshlrev_b32_e32 v186, 5, v3
	v_lshrrev_b32_e32 v3, 2, v0
	v_mul_f32_e32 v2, 0x4f7ffffe, v2
	v_cvt_u32_f32_e32 v2, v2
	v_lshlrev_b32_e32 v12, 8, v11
	v_and_b32_e32 v13, 24, v13
	v_and_b32_e32 v6, 8, v3
	v_readfirstlane_b32 s19, v2
	s_mul_i32 s18, s18, s19
	s_mul_hi_u32 s18, s19, s18
	s_add_i32 s19, s19, s18
	s_mul_hi_u32 s18, s10, s19
	s_mul_i32 s18, s18, s16
	s_sub_i32 s10, s10, s18
	s_sub_i32 s18, s10, s16
	s_cmp_ge_u32 s10, s16
	s_cselect_b32 s10, s18, s10
	s_sub_i32 s18, s10, s16
	s_cmp_ge_u32 s10, s16
	s_cselect_b32 s10, s18, s10
	s_xor_b32 s10, s10, s17
	v_mov_b32_e32 v3, 0
	v_and_b32_e32 v8, 8, v8
	v_and_b32_e32 v4, 4, v4
	s_sub_i32 s34, s10, s17
	v_mbcnt_lo_u32_b32 v2, -1, 0
	v_lshlrev_b32_e32 v1, 4, v1
	v_lshlrev_b32_e32 v184, 5, v14
	s_mov_b32 s11, 0
	v_add3_u32 v188, 0, v12, v13
	v_add_u32_e32 v190, 0x400, v189
	v_mov_b32_e32 v163, v3
	v_mov_b32_e32 v165, v3
	v_cmp_eq_u32_e64 s[6:7], 0, v4
	v_mov_b32_e32 v167, v3
	v_mov_b32_e32 v169, v3
	v_mov_b32_e32 v171, v3
	s_addk_i32 s34, 0x100
	s_mov_b64 s[16:17], -1
	s_movk_i32 s35, 0xc00
	v_lshlrev_b32_e32 v172, 1, v6
	s_add_i32 s40, s27, 0x2000
	s_add_i32 s41, s27, 0x4000
	s_mov_b64 s[18:19], 0x100
	s_add_i32 s54, s27, 0x12000
	s_add_i32 s55, s27, 0x14000
	s_mov_b32 s58, 0x41000000
	v_lshlrev_b32_e32 v174, 1, v8
	v_mbcnt_hi_u32_b32 v191, -1, v2
	v_mov_b32_e32 v248, 0x2000
	v_mov_b32_e32 v249, 0x40000
	v_cndmask_b32_e64 v234, v248, v249, s[2:3]
	v_mov_b32_e32 v235, 0
	v_cndmask_b32_e64 v236, v248, v249, s[4:5]
	v_mov_b32_e32 v237, 0
	v_cndmask_b32_e64 v238, v248, v249, s[6:7]
	v_mov_b32_e32 v239, 0
	s_mov_b32 s84, 0x40000
	s_mov_b32 s85, 0
	v_add_u32_e32 v240, v187, v1
	v_add_u32_e32 v241, v187, v180
	v_add_u32_e32 v242, v187, v181
	v_add_u32_e32 v243, v187, v182
	v_add_u32_e32 v244, 0x12000, v188
	v_add_u32_e32 v245, v244, v184
	v_add_u32_e32 v246, v244, v185
	v_add_u32_e32 v247, v244, v186
	v_add_u32_e32 v244, v244, v183
	s_branch .LBB0_546

; #define LAS __attribute__((address_space(3)))
; DI unsigned pk_bf16(float lo, float hi) { f32x2 v = {lo, hi}; hbf16x2 r = __builtin_convertvector(v, hbf16x2); return __builtin_bit_cast(unsigned, r); }
; #define MFMA32(a, b, c) __builtin_amdgcn_mfma_f32_32x32x16_bf16((a), (b), (c), 0, 0, 0)
;     DI const char* vb(int j) const { return KV + (size_t)keyrow0(j) * 4096 + head * 512 + 256; }
;     DI const char* vb(int q) const { return Z + (size_t)keyrow0(q) * (L1IN * 2) + (1280 + kvh * 128) * 2; }
;     DI const char* vb(int j) const { return Z + (size_t)keyrow0(j) * (L1IN * 2) + (3584 + head * 128) * 2; }
; template <class BiasFn, bool PRE = false>
; DI void at_sm(f32x16& s0, f32x16& s1, f32x16 (&o)[4], float& m, float& l, const float c2, const BiasFn& bias, const int lane, bf16x8 (&pf)[4]) {
;     ...
;     float rs = 0.f;
; #pragma unroll
;     for (int i = 0; i < 16; ++i) { s0[i] = __builtin_amdgcn_exp2f(s0[i]); s1[i] = __builtin_amdgcn_exp2f(s1[i]); rs += s0[i] + s1[i]; }
;     l += rs;
;     u32x4 w;
;     w.x = pk_bf16(s0[0], s0[1]); w.y = pk_bf16(s0[2], s0[3]); w.z = pk_bf16(s0[4], s0[5]); w.w = pk_bf16(s0[6], s0[7]); pf[0] = __builtin_bit_cast(bf16x8, w);
;     w.x = pk_bf16(s0[8], s0[9]); w.y = pk_bf16(s0[10], s0[11]); w.z = pk_bf16(s0[12], s0[13]); w.w = pk_bf16(s0[14], s0[15]); pf[1] = __builtin_bit_cast(bf16x8, w);
;     w.x = pk_bf16(s1[0], s1[1]); w.y = pk_bf16(s1[2], s1[3]); w.z = pk_bf16(s1[4], s1[5]); w.w = pk_bf16(s1[6], s1[7]); pf[2] = __builtin_bit_cast(bf16x8, w);
;     w.x = pk_bf16(s1[8], s1[9]); w.y = pk_bf16(s1[10], s1[11]); w.z = pk_bf16(s1[12], s1[13]); w.w = pk_bf16(s1[14], s1[15]); pf[3] = __builtin_bit_cast(bf16x8, w);
; DI void at_pv(const LAS unsigned char* vs, const AtRd& rd, const bf16x8 (&pf)[4], f32x16 (&o)[4]) {
;     const LAS unsigned char* vb = vs + rd.vbase;
; #pragma unroll
;     for (int ks = 0; ks < 4; ++ks)
; #pragma unroll
;         for (int t = 0; t < 4; ++t) {
;             const s16x4 lo = __builtin_amdgcn_ds_read_tr16_b64_v4i16((LAS s16x4*)(vb + (16 * ks) * 256 + rd.vo[t]));
;             const s16x4 hi = __builtin_amdgcn_ds_read_tr16_b64_v4i16((LAS s16x4*)(vb + (16 * ks + 8) * 256 + rd.vo[t]));
;             const bf16x8 vf = __builtin_shufflevector(lo, hi, 0, 1, 2, 3, 4, 5, 6, 7);
;             o[t] = MFMA32(vf, pf[ks], o[t]);
;         }
; }
.LBB0_555:
	s_cmp_eq_u32 s70, 1
	s_cbranch_scc1 .Lmla_pv1
	s_cmp_eq_u32 s70, 2
	s_cbranch_scc1 .Lmla_pv2
	v_exp_f32_e32 v2, v98
	v_exp_f32_e32 v192, v82
	v_exp_f32_e32 v8, v99
	v_exp_f32_e32 v193, v83
	v_exp_f32_e32 v14, v100
	v_exp_f32_e32 v194, v84
	v_exp_f32_e32 v15, v101
	v_exp_f32_e32 v195, v85
	v_add_f32_e32 v4, v192, v2
	v_exp_f32_e32 v82, v102
	v_exp_f32_e32 v196, v86
	v_add_f32_e32 v4, 0, v4
	v_add_f32_e32 v5, v193, v8
	v_exp_f32_e32 v6, v103
	v_exp_f32_e32 v16, v87
	v_add_f32_e32 v4, v5, v4
	v_add_f32_e32 v5, v194, v14
	v_add_f32_e32 v4, v5, v4
	v_add_f32_e32 v5, v195, v15
	v_add_f32_e32 v7, v5, v4
	v_add_f32_e32 v17, v196, v82
	v_pk_add_f32 v[4:5], v[16:17], v[6:7]
	v_exp_f32_e32 v7, v104
	v_pk_add_f32 v[12:13], v[4:5], v[4:5] op_sel_hi:[0,1]
	v_exp_f32_e32 v17, v88
	v_exp_f32_e32 v12, v105
	v_exp_f32_e32 v98, v89
	v_exp_f32_e32 v197, v90
	v_add_f32_e32 v99, v17, v7
	v_exp_f32_e32 v102, v91
	v_pk_add_f32 v[4:5], v[98:99], v[12:13]
	v_exp_f32_e32 v99, v106
	v_pk_add_f32 v[100:101], v[4:5], v[4:5] op_sel_hi:[0,1]
	v_exp_f32_e32 v100, v107
	v_exp_f32_e32 v106, v93
	v_add_f32_e32 v103, v197, v99
	v_exp_f32_e32 v198, v110
	v_pk_add_f32 v[4:5], v[102:103], v[100:101]
	v_exp_f32_e32 v101, v108
	v_pk_add_f32 v[104:105], v[4:5], v[4:5] op_sel_hi:[0,1]
	v_exp_f32_e32 v103, v92
	v_exp_f32_e32 v104, v109
	v_cvt_pk_bf16_f32 v4, v2, v8
	v_add_f32_e32 v107, v103, v101
	v_pk_add_f32 v[86:87], v[106:107], v[104:105]
	s_nop 0
	ds_read_b64_tr_b16 v[8:9], v244
	ds_read_b64_tr_b16 v[10:11], v244 offset:2048
	v_pk_add_f32 v[108:109], v[86:87], v[86:87] op_sel_hi:[0,1]
	v_exp_f32_e32 v200, v94
	v_cvt_pk_bf16_f32 v5, v14, v15
	v_cvt_pk_bf16_f32 v6, v82, v6
	v_cvt_pk_bf16_f32 v7, v7, v12
	ds_read_b64_tr_b16 v[12:13], v245
	ds_read_b64_tr_b16 v[14:15], v245 offset:2048
	ds_read_b64_tr_b16 v[82:83], v244 offset:4096
	ds_read_b64_tr_b16 v[84:85], v244 offset:6144
	v_exp_f32_e32 v108, v111
	v_exp_f32_e32 v94, v95
	s_waitcnt lgkmcnt(4)
	v_mfma_f32_32x32x16_bf16 v[66:81], v[8:11], v[4:7], v[66:81]
	ds_read_b64_tr_b16 v[8:9], v246
	ds_read_b64_tr_b16 v[10:11], v246 offset:2048
	ds_read_b64_tr_b16 v[86:87], v245 offset:4096
	ds_read_b64_tr_b16 v[88:89], v245 offset:6144
	v_add_f32_e32 v95, v200, v198
	v_pk_add_f32 v[110:111], v[94:95], v[108:109]
	v_exp_f32_e32 v95, v112
	v_pk_add_f32 v[110:111], v[110:111], v[110:111] op_sel_hi:[0,1]
	v_exp_f32_e32 v110, v113
	s_add_i32 s68, s68, 1
	s_waitcnt lgkmcnt(6)
	v_mfma_f32_32x32x16_bf16 v[50:65], v[12:15], v[4:7], v[50:65]
	ds_read_b64_tr_b16 v[12:13], v247
	ds_read_b64_tr_b16 v[14:15], v247 offset:2048
	ds_read_b64_tr_b16 v[90:91], v246 offset:4096
	ds_read_b64_tr_b16 v[92:93], v246 offset:6144
	s_add_i32 s69, s69, 64
	s_cmp_eq_u32 s10, s68
	s_waitcnt lgkmcnt(6)
	v_mfma_f32_32x32x16_bf16 v[34:49], v[8:11], v[4:7], v[34:49]
	ds_read_b64_tr_b16 v[8:9], v247 offset:4096
	ds_read_b64_tr_b16 v[10:11], v247 offset:6144
	s_waitcnt lgkmcnt(4)
	v_mfma_f32_32x32x16_bf16 v[18:33], v[12:15], v[4:7], v[18:33]
	v_cvt_pk_bf16_f32 v4, v99, v100
	v_cvt_pk_bf16_f32 v5, v101, v104
	v_cvt_pk_bf16_f32 v6, v198, v108
	v_cvt_pk_bf16_f32 v7, v95, v110
	s_nop 1
	v_mfma_f32_32x32x16_bf16 v[66:81], v[82:85], v[4:7], v[66:81]
	v_mfma_f32_32x32x16_bf16 v[50:65], v[86:89], v[4:7], v[50:65]
	s_waitcnt lgkmcnt(2)
	v_mfma_f32_32x32x16_bf16 v[34:49], v[90:93], v[4:7], v[34:49]
	s_waitcnt lgkmcnt(0)
	v_mfma_f32_32x32x16_bf16 v[18:33], v[8:11], v[4:7], v[18:33]
	ds_read_b64_tr_b16 v[4:5], v244 offset:8192
	ds_read_b64_tr_b16 v[6:7], v244 offset:10240
	v_cvt_pk_bf16_f32 v8, v192, v193
	v_cvt_pk_bf16_f32 v9, v194, v195
	v_cvt_pk_bf16_f32 v10, v196, v16
	v_cvt_pk_bf16_f32 v11, v17, v98
	ds_read_b64_tr_b16 v[12:13], v244 offset:12288
	ds_read_b64_tr_b16 v[14:15], v244 offset:14336
	s_waitcnt lgkmcnt(2)
	v_mfma_f32_32x32x16_bf16 v[66:81], v[4:7], v[8:11], v[66:81]
	ds_read_b64_tr_b16 v[4:5], v245 offset:8192
	ds_read_b64_tr_b16 v[6:7], v245 offset:10240
	ds_read_b64_tr_b16 v[82:83], v245 offset:12288
	ds_read_b64_tr_b16 v[84:85], v245 offset:14336
	s_waitcnt lgkmcnt(2)
	v_mfma_f32_32x32x16_bf16 v[50:65], v[4:7], v[8:11], v[50:65]
	ds_read_b64_tr_b16 v[4:5], v246 offset:8192
	ds_read_b64_tr_b16 v[6:7], v246 offset:10240
	ds_read_b64_tr_b16 v[86:87], v246 offset:12288
	ds_read_b64_tr_b16 v[88:89], v246 offset:14336
	s_waitcnt lgkmcnt(2)
	v_mfma_f32_32x32x16_bf16 v[34:49], v[4:7], v[8:11], v[34:49]
	ds_read_b64_tr_b16 v[4:5], v247 offset:8192
	ds_read_b64_tr_b16 v[6:7], v247 offset:10240
	ds_read_b64_tr_b16 v[90:91], v247 offset:12288
	ds_read_b64_tr_b16 v[92:93], v247 offset:14336
	v_exp_f32_e32 v2, v96
	s_cbranch_scc1 .Lmla_w0_0
	s_waitcnt vmcnt(5)
	s_branch .Lmla_wd_0

; template <class BiasFn, bool PRE = false>
; DI void at_sm(f32x16& s0, f32x16& s1, f32x16 (&o)[4], float& m, float& l, const float c2, const BiasFn& bias, const int lane, bf16x8 (&pf)[4]) {
;     ...
;     float rs = 0.f;
; #pragma unroll
;     for (int i = 0; i < 16; ++i) { s0[i] = __builtin_amdgcn_exp2f(s0[i]); s1[i] = __builtin_amdgcn_exp2f(s1[i]); rs += s0[i] + s1[i]; }
;     l += rs;
;     u32x4 w;
;     w.x = pk_bf16(s0[0], s0[1]); w.y = pk_bf16(s0[2], s0[3]); w.z = pk_bf16(s0[4], s0[5]); w.w = pk_bf16(s0[6], s0[7]); pf[0] = __builtin_bit_cast(bf16x8, w);
;     w.x = pk_bf16(s0[8], s0[9]); w.y = pk_bf16(s0[10], s0[11]); w.z = pk_bf16(s0[12], s0[13]); w.w = pk_bf16(s0[14], s0[15]); pf[1] = __builtin_bit_cast(bf16x8, w);
;     w.x = pk_bf16(s1[0], s1[1]); w.y = pk_bf16(s1[2], s1[3]); w.z = pk_bf16(s1[4], s1[5]); w.w = pk_bf16(s1[6], s1[7]); pf[2] = __builtin_bit_cast(bf16x8, w);
;     w.x = pk_bf16(s1[8], s1[9]); w.y = pk_bf16(s1[10], s1[11]); w.z = pk_bf16(s1[12], s1[13]); w.w = pk_bf16(s1[14], s1[15]); pf[3] = __builtin_bit_cast(bf16x8, w);
; }
; DI void at_pv(const LAS unsigned char* vs, const AtRd& rd, const bf16x8 (&pf)[4], f32x16 (&o)[4]) {
;     const LAS unsigned char* vb = vs + rd.vbase;
; #pragma unroll
;     for (int ks = 0; ks < 4; ++ks)
; #pragma unroll
;         for (int t = 0; t < 4; ++t) {
;             const s16x4 lo = __builtin_amdgcn_ds_read_tr16_b64_v4i16((LAS s16x4*)(vb + (16 * ks) * 256 + rd.vo[t]));
;             const s16x4 hi = __builtin_amdgcn_ds_read_tr16_b64_v4i16((LAS s16x4*)(vb + (16 * ks + 8) * 256 + rd.vo[t]));
;             const bf16x8 vf = __builtin_shufflevector(lo, hi, 0, 1, 2, 3, 4, 5, 6, 7);
;             o[t] = MFMA32(vf, pf[ks], o[t]);
;         }
; }
; template <int DQ, class Drv>
; DI void at_run3(LAS unsigned char* lds, const Drv& D, const int n, const AtRd& rd, const AtDma& dm, const bf16x8 (&qf)[DQ / 16], f32x16 (&o)[4], float& m, float& l, const float c2, const int lane, const int wave) {
;     ...
;             at_sm_pv(lds + cur * AT4_SLOT + AT_KSLOT, rd, a0, a1, o, m, l, c2, D.bias(j), lane);
;         }
;         if (j + 2 < n) { if (DQ == 192) asm volatile("s_waitcnt vmcnt(5)" ::: "memory"); else asm volatile("s_waitcnt vmcnt(4)" ::: "memory"); }
;         else asm volatile("s_waitcnt vmcnt(0)" ::: "memory");
;         __syncthreads();
;         cur = cur == 2 ? 0 : cur + 1;
.Lmla_wd_0:
	s_waitcnt lgkmcnt(0)
	s_barrier
	v_mfma_f32_32x32x16_bf16 v[18:33], v[4:7], v[8:11], v[18:33]
	v_exp_f32_e32 v8, v97
	v_cvt_pk_bf16_f32 v4, v197, v102
	v_cvt_pk_bf16_f32 v5, v103, v106
	v_cvt_pk_bf16_f32 v6, v200, v94
	v_cvt_pk_bf16_f32 v7, v2, v8
	v_add_f32_e32 v9, v2, v95
	v_pk_add_f32 v[8:9], v[8:9], v[110:111]
	v_mfma_f32_32x32x16_bf16 v[66:81], v[12:15], v[4:7], v[66:81]
	v_add_f32_e32 v2, v8, v9
	v_add_f32_e32 v173, v173, v2
	v_mfma_f32_32x32x16_bf16 v[50:65], v[82:85], v[4:7], v[50:65]
	v_mfma_f32_32x32x16_bf16 v[34:49], v[86:89], v[4:7], v[34:49]
	v_mfma_f32_32x32x16_bf16 v[18:33], v[90:93], v[4:7], v[18:33]
	s_cbranch_scc1 .LBB0_558
	s_branch .LBB0_556
.Lmla_pv1:
	v_exp_f32_e32 v2, v98
	v_exp_f32_e32 v192, v82
	v_exp_f32_e32 v8, v99
	v_exp_f32_e32 v193, v83
	v_exp_f32_e32 v14, v100
	v_exp_f32_e32 v194, v84
	v_exp_f32_e32 v15, v101
	v_exp_f32_e32 v195, v85
	v_add_f32_e32 v4, v192, v2
	v_exp_f32_e32 v82, v102
	v_exp_f32_e32 v196, v86
	v_add_f32_e32 v4, 0, v4
	v_add_f32_e32 v5, v193, v8
	v_exp_f32_e32 v6, v103
	v_exp_f32_e32 v16, v87
	v_add_f32_e32 v4, v5, v4
	v_add_f32_e32 v5, v194, v14
	v_add_f32_e32 v4, v5, v4
	v_add_f32_e32 v5, v195, v15
	v_add_f32_e32 v7, v5, v4
	v_add_f32_e32 v17, v196, v82
	v_pk_add_f32 v[4:5], v[16:17], v[6:7]
	v_exp_f32_e32 v7, v104
	v_pk_add_f32 v[12:13], v[4:5], v[4:5] op_sel_hi:[0,1]
	v_exp_f32_e32 v17, v88
	v_exp_f32_e32 v12, v105
	v_exp_f32_e32 v98, v89
	v_exp_f32_e32 v197, v90
	v_add_f32_e32 v99, v17, v7
	v_exp_f32_e32 v102, v91
	v_pk_add_f32 v[4:5], v[98:99], v[12:13]
	v_exp_f32_e32 v99, v106
	v_pk_add_f32 v[100:101], v[4:5], v[4:5] op_sel_hi:[0,1]
	v_exp_f32_e32 v100, v107
	v_exp_f32_e32 v106, v93
	v_add_f32_e32 v103, v197, v99
	v_exp_f32_e32 v198, v110
	v_pk_add_f32 v[4:5], v[102:103], v[100:101]
	v_exp_f32_e32 v101, v108
	v_pk_add_f32 v[104:105], v[4:5], v[4:5] op_sel_hi:[0,1]
	v_exp_f32_e32 v103, v92
	v_exp_f32_e32 v104, v109
	v_cvt_pk_bf16_f32 v4, v2, v8
	v_add_f32_e32 v107, v103, v101
	v_pk_add_f32 v[86:87], v[106:107], v[104:105]
	s_nop 0
	ds_read_b64_tr_b16 v[8:9], v244 offset:16384
	ds_read_b64_tr_b16 v[10:11], v244 offset:18432
	v_pk_add_f32 v[108:109], v[86:87], v[86:87] op_sel_hi:[0,1]
	v_exp_f32_e32 v200, v94
	v_cvt_pk_bf16_f32 v5, v14, v15
	v_cvt_pk_bf16_f32 v6, v82, v6
	v_cvt_pk_bf16_f32 v7, v7, v12
	ds_read_b64_tr_b16 v[12:13], v245 offset:16384
	ds_read_b64_tr_b16 v[14:15], v245 offset:18432
	ds_read_b64_tr_b16 v[82:83], v244 offset:20480
	ds_read_b64_tr_b16 v[84:85], v244 offset:22528
	v_exp_f32_e32 v108, v111
	v_exp_f32_e32 v94, v95
	s_waitcnt lgkmcnt(4)
	v_mfma_f32_32x32x16_bf16 v[66:81], v[8:11], v[4:7], v[66:81]
	ds_read_b64_tr_b16 v[8:9], v246 offset:16384
	ds_read_b64_tr_b16 v[10:11], v246 offset:18432
	ds_read_b64_tr_b16 v[86:87], v245 offset:20480
	ds_read_b64_tr_b16 v[88:89], v245 offset:22528
	v_add_f32_e32 v95, v200, v198
	v_pk_add_f32 v[110:111], v[94:95], v[108:109]
	v_exp_f32_e32 v95, v112
	v_pk_add_f32 v[110:111], v[110:111], v[110:111] op_sel_hi:[0,1]
	v_exp_f32_e32 v110, v113
	s_add_i32 s68, s68, 1
	s_waitcnt lgkmcnt(6)
	v_mfma_f32_32x32x16_bf16 v[50:65], v[12:15], v[4:7], v[50:65]
	ds_read_b64_tr_b16 v[12:13], v247 offset:16384
	ds_read_b64_tr_b16 v[14:15], v247 offset:18432
	ds_read_b64_tr_b16 v[90:91], v246 offset:20480
	ds_read_b64_tr_b16 v[92:93], v246 offset:22528
	s_add_i32 s69, s69, 64
	s_cmp_eq_u32 s10, s68
	s_waitcnt lgkmcnt(6)
	v_mfma_f32_32x32x16_bf16 v[34:49], v[8:11], v[4:7], v[34:49]
	ds_read_b64_tr_b16 v[8:9], v247 offset:20480
	ds_read_b64_tr_b16 v[10:11], v247 offset:22528
	s_waitcnt lgkmcnt(4)
	v_mfma_f32_32x32x16_bf16 v[18:33], v[12:15], v[4:7], v[18:33]
	v_cvt_pk_bf16_f32 v4, v99, v100
	v_cvt_pk_bf16_f32 v5, v101, v104
	v_cvt_pk_bf16_f32 v6, v198, v108
	v_cvt_pk_bf16_f32 v7, v95, v110
	s_nop 1
	v_mfma_f32_32x32x16_bf16 v[66:81], v[82:85], v[4:7], v[66:81]
	v_mfma_f32_32x32x16_bf16 v[50:65], v[86:89], v[4:7], v[50:65]
	s_waitcnt lgkmcnt(2)
	v_mfma_f32_32x32x16_bf16 v[34:49], v[90:93], v[4:7], v[34:49]
	s_waitcnt lgkmcnt(0)
	v_mfma_f32_32x32x16_bf16 v[18:33], v[8:11], v[4:7], v[18:33]
	ds_read_b64_tr_b16 v[4:5], v244 offset:24576
	ds_read_b64_tr_b16 v[6:7], v244 offset:26624
	v_cvt_pk_bf16_f32 v8, v192, v193
	v_cvt_pk_bf16_f32 v9, v194, v195
	v_cvt_pk_bf16_f32 v10, v196, v16
	v_cvt_pk_bf16_f32 v11, v17, v98
	ds_read_b64_tr_b16 v[12:13], v244 offset:28672
	ds_read_b64_tr_b16 v[14:15], v244 offset:30720
	s_waitcnt lgkmcnt(2)
	v_mfma_f32_32x32x16_bf16 v[66:81], v[4:7], v[8:11], v[66:81]
	ds_read_b64_tr_b16 v[4:5], v245 offset:24576
	ds_read_b64_tr_b16 v[6:7], v245 offset:26624
	ds_read_b64_tr_b16 v[82:83], v245 offset:28672
	ds_read_b64_tr_b16 v[84:85], v245 offset:30720
	s_waitcnt lgkmcnt(2)
	v_mfma_f32_32x32x16_bf16 v[50:65], v[4:7], v[8:11], v[50:65]
	ds_read_b64_tr_b16 v[4:5], v246 offset:24576
	ds_read_b64_tr_b16 v[6:7], v246 offset:26624
	ds_read_b64_tr_b16 v[86:87], v246 offset:28672
	ds_read_b64_tr_b16 v[88:89], v246 offset:30720
	s_waitcnt lgkmcnt(2)
	v_mfma_f32_32x32x16_bf16 v[34:49], v[4:7], v[8:11], v[34:49]
	ds_read_b64_tr_b16 v[4:5], v247 offset:24576
	ds_read_b64_tr_b16 v[6:7], v247 offset:26624
	ds_read_b64_tr_b16 v[90:91], v247 offset:28672
	ds_read_b64_tr_b16 v[92:93], v247 offset:30720
	v_exp_f32_e32 v2, v96
	s_cbranch_scc1 .Lmla_w0_1
	s_waitcnt vmcnt(5)
	s_branch .Lmla_wd_1

; #define LAS __attribute__((address_space(3)))
; DI unsigned pk_bf16(float lo, float hi) { f32x2 v = {lo, hi}; hbf16x2 r = __builtin_convertvector(v, hbf16x2); return __builtin_bit_cast(unsigned, r); }
; #define MFMA32(a, b, c) __builtin_amdgcn_mfma_f32_32x32x16_bf16((a), (b), (c), 0, 0, 0)
;     DI const char* vb(int j) const { return KV + (size_t)keyrow0(j) * 4096 + head * 512 + 256; }
;     DI const char* vb(int q) const { return Z + (size_t)keyrow0(q) * (L1IN * 2) + (1280 + kvh * 128) * 2; }
;     DI const char* vb(int j) const { return Z + (size_t)keyrow0(j) * (L1IN * 2) + (3584 + head * 128) * 2; }
; template <class BiasFn, bool PRE = false>
; DI void at_sm(f32x16& s0, f32x16& s1, f32x16 (&o)[4], float& m, float& l, const float c2, const BiasFn& bias, const int lane, bf16x8 (&pf)[4]) {
;     ...
;     float rs = 0.f;
; #pragma unroll
;     for (int i = 0; i < 16; ++i) { s0[i] = __builtin_amdgcn_exp2f(s0[i]); s1[i] = __builtin_amdgcn_exp2f(s1[i]); rs += s0[i] + s1[i]; }
;     l += rs;
;     u32x4 w;
;     w.x = pk_bf16(s0[0], s0[1]); w.y = pk_bf16(s0[2], s0[3]); w.z = pk_bf16(s0[4], s0[5]); w.w = pk_bf16(s0[6], s0[7]); pf[0] = __builtin_bit_cast(bf16x8, w);
;     w.x = pk_bf16(s0[8], s0[9]); w.y = pk_bf16(s0[10], s0[11]); w.z = pk_bf16(s0[12], s0[13]); w.w = pk_bf16(s0[14], s0[15]); pf[1] = __builtin_bit_cast(bf16x8, w);
;     w.x = pk_bf16(s1[0], s1[1]); w.y = pk_bf16(s1[2], s1[3]); w.z = pk_bf16(s1[4], s1[5]); w.w = pk_bf16(s1[6], s1[7]); pf[2] = __builtin_bit_cast(bf16x8, w);
;     w.x = pk_bf16(s1[8], s1[9]); w.y = pk_bf16(s1[10], s1[11]); w.z = pk_bf16(s1[12], s1[13]); w.w = pk_bf16(s1[14], s1[15]); pf[3] = __builtin_bit_cast(bf16x8, w);
; DI void at_pv(const LAS unsigned char* vs, const AtRd& rd, const bf16x8 (&pf)[4], f32x16 (&o)[4]) {
;     const LAS unsigned char* vb = vs + rd.vbase;
; #pragma unroll
;     for (int ks = 0; ks < 4; ++ks)
; #pragma unroll
;         for (int t = 0; t < 4; ++t) {
;             const s16x4 lo = __builtin_amdgcn_ds_read_tr16_b64_v4i16((LAS s16x4*)(vb + (16 * ks) * 256 + rd.vo[t]));
;             const s16x4 hi = __builtin_amdgcn_ds_read_tr16_b64_v4i16((LAS s16x4*)(vb + (16 * ks + 8) * 256 + rd.vo[t]));
;             const bf16x8 vf = __builtin_shufflevector(lo, hi, 0, 1, 2, 3, 4, 5, 6, 7);
;             o[t] = MFMA32(vf, pf[ks], o[t]);
;         }
; }
.Lmla_pv2:
	v_exp_f32_e32 v2, v98
	v_exp_f32_e32 v192, v82
	v_exp_f32_e32 v8, v99
	v_exp_f32_e32 v193, v83
	v_exp_f32_e32 v14, v100
	v_exp_f32_e32 v194, v84
	v_exp_f32_e32 v15, v101
	v_exp_f32_e32 v195, v85
	v_add_f32_e32 v4, v192, v2
	v_exp_f32_e32 v82, v102
	v_exp_f32_e32 v196, v86
	v_add_f32_e32 v4, 0, v4
	v_add_f32_e32 v5, v193, v8
	v_exp_f32_e32 v6, v103
	v_exp_f32_e32 v16, v87
	v_add_f32_e32 v4, v5, v4
	v_add_f32_e32 v5, v194, v14
	v_add_f32_e32 v4, v5, v4
	v_add_f32_e32 v5, v195, v15
	v_add_f32_e32 v7, v5, v4
	v_add_f32_e32 v17, v196, v82
	v_pk_add_f32 v[4:5], v[16:17], v[6:7]
	v_exp_f32_e32 v7, v104
	v_pk_add_f32 v[12:13], v[4:5], v[4:5] op_sel_hi:[0,1]
	v_exp_f32_e32 v17, v88
	v_exp_f32_e32 v12, v105
	v_exp_f32_e32 v98, v89
	v_exp_f32_e32 v197, v90
	v_add_f32_e32 v99, v17, v7
	v_exp_f32_e32 v102, v91
	v_pk_add_f32 v[4:5], v[98:99], v[12:13]
	v_exp_f32_e32 v99, v106
	v_pk_add_f32 v[100:101], v[4:5], v[4:5] op_sel_hi:[0,1]
	v_exp_f32_e32 v100, v107
	v_exp_f32_e32 v106, v93
	v_add_f32_e32 v103, v197, v99
	v_exp_f32_e32 v198, v110
	v_pk_add_f32 v[4:5], v[102:103], v[100:101]
	v_exp_f32_e32 v101, v108
	v_pk_add_f32 v[104:105], v[4:5], v[4:5] op_sel_hi:[0,1]
	v_exp_f32_e32 v103, v92
	v_exp_f32_e32 v104, v109
	v_cvt_pk_bf16_f32 v4, v2, v8
	v_add_f32_e32 v107, v103, v101
	v_pk_add_f32 v[86:87], v[106:107], v[104:105]
	s_nop 0
	ds_read_b64_tr_b16 v[8:9], v244 offset:32768
	ds_read_b64_tr_b16 v[10:11], v244 offset:34816
	v_pk_add_f32 v[108:109], v[86:87], v[86:87] op_sel_hi:[0,1]
	v_exp_f32_e32 v200, v94
	v_cvt_pk_bf16_f32 v5, v14, v15
	v_cvt_pk_bf16_f32 v6, v82, v6
	v_cvt_pk_bf16_f32 v7, v7, v12
	ds_read_b64_tr_b16 v[12:13], v245 offset:32768
	ds_read_b64_tr_b16 v[14:15], v245 offset:34816
	ds_read_b64_tr_b16 v[82:83], v244 offset:36864
	ds_read_b64_tr_b16 v[84:85], v244 offset:38912
	v_exp_f32_e32 v108, v111
	v_exp_f32_e32 v94, v95
	s_waitcnt lgkmcnt(4)
	v_mfma_f32_32x32x16_bf16 v[66:81], v[8:11], v[4:7], v[66:81]
	ds_read_b64_tr_b16 v[8:9], v246 offset:32768
	ds_read_b64_tr_b16 v[10:11], v246 offset:34816
	ds_read_b64_tr_b16 v[86:87], v245 offset:36864
	ds_read_b64_tr_b16 v[88:89], v245 offset:38912
	v_add_f32_e32 v95, v200, v198
	v_pk_add_f32 v[110:111], v[94:95], v[108:109]
	v_exp_f32_e32 v95, v112
	v_pk_add_f32 v[110:111], v[110:111], v[110:111] op_sel_hi:[0,1]
	v_exp_f32_e32 v110, v113
	s_add_i32 s68, s68, 1
	s_waitcnt lgkmcnt(6)
	v_mfma_f32_32x32x16_bf16 v[50:65], v[12:15], v[4:7], v[50:65]
	ds_read_b64_tr_b16 v[12:13], v247 offset:32768
	ds_read_b64_tr_b16 v[14:15], v247 offset:34816
	ds_read_b64_tr_b16 v[90:91], v246 offset:36864
	ds_read_b64_tr_b16 v[92:93], v246 offset:38912
	s_add_i32 s69, s69, 64
	s_cmp_eq_u32 s10, s68
	s_waitcnt lgkmcnt(6)
	v_mfma_f32_32x32x16_bf16 v[34:49], v[8:11], v[4:7], v[34:49]
	ds_read_b64_tr_b16 v[8:9], v247 offset:36864
	ds_read_b64_tr_b16 v[10:11], v247 offset:38912
	s_waitcnt lgkmcnt(4)
	v_mfma_f32_32x32x16_bf16 v[18:33], v[12:15], v[4:7], v[18:33]
	v_cvt_pk_bf16_f32 v4, v99, v100
	v_cvt_pk_bf16_f32 v5, v101, v104
	v_cvt_pk_bf16_f32 v6, v198, v108
	v_cvt_pk_bf16_f32 v7, v95, v110
	s_nop 1
	v_mfma_f32_32x32x16_bf16 v[66:81], v[82:85], v[4:7], v[66:81]
	v_mfma_f32_32x32x16_bf16 v[50:65], v[86:89], v[4:7], v[50:65]
	s_waitcnt lgkmcnt(2)
	v_mfma_f32_32x32x16_bf16 v[34:49], v[90:93], v[4:7], v[34:49]
	s_waitcnt lgkmcnt(0)
	v_mfma_f32_32x32x16_bf16 v[18:33], v[8:11], v[4:7], v[18:33]
	ds_read_b64_tr_b16 v[4:5], v244 offset:40960
	ds_read_b64_tr_b16 v[6:7], v244 offset:43008
	v_cvt_pk_bf16_f32 v8, v192, v193
	v_cvt_pk_bf16_f32 v9, v194, v195
	v_cvt_pk_bf16_f32 v10, v196, v16
	v_cvt_pk_bf16_f32 v11, v17, v98
	ds_read_b64_tr_b16 v[12:13], v244 offset:45056
	ds_read_b64_tr_b16 v[14:15], v244 offset:47104
	s_waitcnt lgkmcnt(2)
	v_mfma_f32_32x32x16_bf16 v[66:81], v[4:7], v[8:11], v[66:81]
	ds_read_b64_tr_b16 v[4:5], v245 offset:40960
	ds_read_b64_tr_b16 v[6:7], v245 offset:43008
	ds_read_b64_tr_b16 v[82:83], v245 offset:45056
	ds_read_b64_tr_b16 v[84:85], v245 offset:47104
	s_waitcnt lgkmcnt(2)
	v_mfma_f32_32x32x16_bf16 v[50:65], v[4:7], v[8:11], v[50:65]
	ds_read_b64_tr_b16 v[4:5], v246 offset:40960
	ds_read_b64_tr_b16 v[6:7], v246 offset:43008
	ds_read_b64_tr_b16 v[86:87], v246 offset:45056
	ds_read_b64_tr_b16 v[88:89], v246 offset:47104
	s_waitcnt lgkmcnt(2)
	v_mfma_f32_32x32x16_bf16 v[34:49], v[4:7], v[8:11], v[34:49]
	ds_read_b64_tr_b16 v[4:5], v247 offset:40960
	ds_read_b64_tr_b16 v[6:7], v247 offset:43008
	ds_read_b64_tr_b16 v[90:91], v247 offset:45056
	ds_read_b64_tr_b16 v[92:93], v247 offset:47104
	v_exp_f32_e32 v2, v96
	s_cbranch_scc1 .Lmla_w0_2
	s_waitcnt vmcnt(5)
	s_branch .Lmla_wd_2

; #define LAS __attribute__((address_space(3)))
; #define MFMA32(a, b, c) __builtin_amdgcn_mfma_f32_32x32x16_bf16((a), (b), (c), 0, 0, 0)
; #pragma unroll
;     for (int i = 0; i < 16; ++i) { s0[i] = init; s1[i] = init; }
;     const LAS unsigned char* kp0 = ks + rd.kbase; const LAS unsigned char* kp1 = ks + rd.kbase1;
; #pragma unroll
;     for (int s = 0; s < DQ / 16; ++s) {
;         const LAS unsigned char* kp = (DQ == 128) ? ((s >> 2) ? kp1 : kp0) : kp0 + ((s >> 2) << 7);
;         const bf16x8 a0 = *(const LAS bf16x8*)(kp + rd.ko[s & 3]);
;         const bf16x8 a1 = *(const LAS bf16x8*)(kp + 32 * (DQ * 2) + rd.ko[s & 3]);
;         s0 = MFMA32(a0, qf[s], s0); s1 = MFMA32(a1, qf[s], s1);
;     }
; }
.Lmla_nodma:
	s_cmp_eq_u32 s70, 1
	s_cbranch_scc1 .Lmla_qk1
	s_cmp_eq_u32 s70, 2
	s_cbranch_scc1 .Lmla_qk2
	ds_read_b128 v[4:7], v240
	ds_read_b128 v[8:11], v240 offset:128
	v_xor_b32_e32 v82, 0x80000000, v179
	v_mov_b32_e32 v83, v82
	v_mov_b64_e32 v[84:85], v[82:83]
	v_mov_b64_e32 v[86:87], v[82:83]
	v_mov_b64_e32 v[88:89], v[82:83]
	v_mov_b64_e32 v[90:91], v[82:83]
	v_mov_b64_e32 v[92:93], v[82:83]
	v_mov_b64_e32 v[94:95], v[82:83]
	v_mov_b64_e32 v[96:97], v[82:83]
	s_nop 0
	s_waitcnt lgkmcnt(0)
	v_mfma_f32_32x32x16_bf16 v[98:113], v[4:7], v[158:161], v[82:97]
	ds_read_b128 v[4:7], v240 offset:12288
	ds_read_b128 v[12:15], v240 offset:256
	s_waitcnt lgkmcnt(0)
	v_mfma_f32_32x32x16_bf16 v[82:97], v[4:7], v[158:161], v[82:97]
	ds_read_b128 v[4:7], v241
	ds_read_b128 v[192:195], v241 offset:128
	s_waitcnt lgkmcnt(0)
	v_mfma_f32_32x32x16_bf16 v[98:113], v[4:7], v[154:157], v[98:113]
	ds_read_b128 v[4:7], v241 offset:12288
	ds_read_b128 v[196:199], v241 offset:256
	s_waitcnt lgkmcnt(0)
	v_mfma_f32_32x32x16_bf16 v[82:97], v[4:7], v[154:157], v[82:97]
	ds_read_b128 v[4:7], v242
	ds_read_b128 v[200:203], v242 offset:128
	s_waitcnt lgkmcnt(0)
	v_mfma_f32_32x32x16_bf16 v[98:113], v[4:7], v[150:153], v[98:113]
	ds_read_b128 v[4:7], v242 offset:12288
	ds_read_b128 v[204:207], v242 offset:256
	s_waitcnt lgkmcnt(0)
	v_mfma_f32_32x32x16_bf16 v[82:97], v[4:7], v[150:153], v[82:97]
	ds_read_b128 v[4:7], v243
	ds_read_b128 v[208:211], v243 offset:128
	s_waitcnt lgkmcnt(0)
	v_mfma_f32_32x32x16_bf16 v[98:113], v[4:7], v[146:149], v[98:113]
	ds_read_b128 v[4:7], v243 offset:12288
	ds_read_b128 v[212:215], v243 offset:256
	s_waitcnt lgkmcnt(0)
	v_mfma_f32_32x32x16_bf16 v[82:97], v[4:7], v[146:149], v[82:97]
	v_mfma_f32_32x32x16_bf16 v[98:113], v[8:11], v[142:145], v[98:113]
	ds_read_b128 v[4:7], v240 offset:12416
	ds_read_b128 v[8:11], v240 offset:12544
	s_waitcnt lgkmcnt(0)
	v_mfma_f32_32x32x16_bf16 v[82:97], v[4:7], v[142:145], v[82:97]
	v_mfma_f32_32x32x16_bf16 v[98:113], v[192:195], v[138:141], v[98:113]
	ds_read_b128 v[4:7], v241 offset:12416
	ds_read_b128 v[192:195], v241 offset:12544
	s_waitcnt lgkmcnt(0)
	v_mfma_f32_32x32x16_bf16 v[82:97], v[4:7], v[138:141], v[82:97]
	v_mfma_f32_32x32x16_bf16 v[98:113], v[200:203], v[134:137], v[98:113]
	ds_read_b128 v[4:7], v242 offset:12416
	ds_read_b128 v[200:203], v242 offset:12544
	s_waitcnt lgkmcnt(0)
	v_mfma_f32_32x32x16_bf16 v[82:97], v[4:7], v[134:137], v[82:97]
	v_mfma_f32_32x32x16_bf16 v[98:113], v[208:211], v[130:133], v[98:113]
	ds_read_b128 v[4:7], v243 offset:12416
	ds_read_b128 v[208:211], v243 offset:12544
	s_waitcnt lgkmcnt(0)
	v_mfma_f32_32x32x16_bf16 v[82:97], v[4:7], v[130:133], v[82:97]
	v_mfma_f32_32x32x16_bf16 v[98:113], v[12:15], v[126:129], v[98:113]
	v_mfma_f32_32x32x16_bf16 v[82:97], v[8:11], v[126:129], v[82:97]
	v_mfma_f32_32x32x16_bf16 v[98:113], v[196:199], v[122:125], v[98:113]
	v_mfma_f32_32x32x16_bf16 v[82:97], v[192:195], v[122:125], v[82:97]
	v_mfma_f32_32x32x16_bf16 v[98:113], v[204:207], v[118:121], v[98:113]
	v_mfma_f32_32x32x16_bf16 v[82:97], v[200:203], v[118:121], v[82:97]
	v_mfma_f32_32x32x16_bf16 v[98:113], v[212:215], v[114:117], v[98:113]
	v_mfma_f32_32x32x16_bf16 v[82:97], v[208:211], v[114:117], v[82:97]
	s_branch .Lmla_qkd
.Lmla_qk1:
	ds_read_b128 v[4:7], v240 offset:24576
	ds_read_b128 v[8:11], v240 offset:24704
	v_xor_b32_e32 v82, 0x80000000, v179
	v_mov_b32_e32 v83, v82
	v_mov_b64_e32 v[84:85], v[82:83]
	v_mov_b64_e32 v[86:87], v[82:83]
	v_mov_b64_e32 v[88:89], v[82:83]
	v_mov_b64_e32 v[90:91], v[82:83]
	v_mov_b64_e32 v[92:93], v[82:83]
	v_mov_b64_e32 v[94:95], v[82:83]
	v_mov_b64_e32 v[96:97], v[82:83]
	s_nop 0
	s_waitcnt lgkmcnt(0)
	v_mfma_f32_32x32x16_bf16 v[98:113], v[4:7], v[158:161], v[82:97]
	ds_read_b128 v[4:7], v240 offset:36864
	ds_read_b128 v[12:15], v240 offset:24832
	s_waitcnt lgkmcnt(0)
	v_mfma_f32_32x32x16_bf16 v[82:97], v[4:7], v[158:161], v[82:97]
	ds_read_b128 v[4:7], v241 offset:24576
	ds_read_b128 v[192:195], v241 offset:24704
	s_waitcnt lgkmcnt(0)
	v_mfma_f32_32x32x16_bf16 v[98:113], v[4:7], v[154:157], v[98:113]
	ds_read_b128 v[4:7], v241 offset:36864
	ds_read_b128 v[196:199], v241 offset:24832
	s_waitcnt lgkmcnt(0)
	v_mfma_f32_32x32x16_bf16 v[82:97], v[4:7], v[154:157], v[82:97]
	ds_read_b128 v[4:7], v242 offset:24576
	ds_read_b128 v[200:203], v242 offset:24704
	s_waitcnt lgkmcnt(0)
	v_mfma_f32_32x32x16_bf16 v[98:113], v[4:7], v[150:153], v[98:113]
	ds_read_b128 v[4:7], v242 offset:36864
	ds_read_b128 v[204:207], v242 offset:24832
	s_waitcnt lgkmcnt(0)
	v_mfma_f32_32x32x16_bf16 v[82:97], v[4:7], v[150:153], v[82:97]
	ds_read_b128 v[4:7], v243 offset:24576
	ds_read_b128 v[208:211], v243 offset:24704
	s_waitcnt lgkmcnt(0)
	v_mfma_f32_32x32x16_bf16 v[98:113], v[4:7], v[146:149], v[98:113]
	ds_read_b128 v[4:7], v243 offset:36864
	ds_read_b128 v[212:215], v243 offset:24832
	s_waitcnt lgkmcnt(0)
	v_mfma_f32_32x32x16_bf16 v[82:97], v[4:7], v[146:149], v[82:97]
	v_mfma_f32_32x32x16_bf16 v[98:113], v[8:11], v[142:145], v[98:113]
	ds_read_b128 v[4:7], v240 offset:36992
	ds_read_b128 v[8:11], v240 offset:37120
	s_waitcnt lgkmcnt(0)
	v_mfma_f32_32x32x16_bf16 v[82:97], v[4:7], v[142:145], v[82:97]
	v_mfma_f32_32x32x16_bf16 v[98:113], v[192:195], v[138:141], v[98:113]
	ds_read_b128 v[4:7], v241 offset:36992
	ds_read_b128 v[192:195], v241 offset:37120
	s_waitcnt lgkmcnt(0)
	v_mfma_f32_32x32x16_bf16 v[82:97], v[4:7], v[138:141], v[82:97]
	v_mfma_f32_32x32x16_bf16 v[98:113], v[200:203], v[134:137], v[98:113]
	ds_read_b128 v[4:7], v242 offset:36992
	ds_read_b128 v[200:203], v242 offset:37120
	s_waitcnt lgkmcnt(0)
	v_mfma_f32_32x32x16_bf16 v[82:97], v[4:7], v[134:137], v[82:97]
	v_mfma_f32_32x32x16_bf16 v[98:113], v[208:211], v[130:133], v[98:113]
	ds_read_b128 v[4:7], v243 offset:36992
	ds_read_b128 v[208:211], v243 offset:37120
	s_waitcnt lgkmcnt(0)
	v_mfma_f32_32x32x16_bf16 v[82:97], v[4:7], v[130:133], v[82:97]
	v_mfma_f32_32x32x16_bf16 v[98:113], v[12:15], v[126:129], v[98:113]
	v_mfma_f32_32x32x16_bf16 v[82:97], v[8:11], v[126:129], v[82:97]
	v_mfma_f32_32x32x16_bf16 v[98:113], v[196:199], v[122:125], v[98:113]
	v_mfma_f32_32x32x16_bf16 v[82:97], v[192:195], v[122:125], v[82:97]
	v_mfma_f32_32x32x16_bf16 v[98:113], v[204:207], v[118:121], v[98:113]
	v_mfma_f32_32x32x16_bf16 v[82:97], v[200:203], v[118:121], v[82:97]
	v_mfma_f32_32x32x16_bf16 v[98:113], v[212:215], v[114:117], v[98:113]
	v_mfma_f32_32x32x16_bf16 v[82:97], v[208:211], v[114:117], v[82:97]
	s_branch .Lmla_qkd
; #define LAS __attribute__((address_space(3)))
; #define MFMA32(a, b, c) __builtin_amdgcn_mfma_f32_32x32x16_bf16((a), (b), (c), 0, 0, 0)
;     DI NoBias bias(int) const { return NoBias(); }
;     DI WinBias bias(int q) const { const int j = tid_(q); WinBias B; B.base = j < 4 ? 100 : qpos - (k0base + 64 * (j - 4)) + 128; return B; }
; #pragma unroll
;     for (int i = 0; i < 16; ++i) { s0[i] = init; s1[i] = init; }
;     const LAS unsigned char* kp0 = ks + rd.kbase; const LAS unsigned char* kp1 = ks + rd.kbase1;
; #pragma unroll
;     for (int s = 0; s < DQ / 16; ++s) {
;         const LAS unsigned char* kp = (DQ == 128) ? ((s >> 2) ? kp1 : kp0) : kp0 + ((s >> 2) << 7);
;         const bf16x8 a0 = *(const LAS bf16x8*)(kp + rd.ko[s & 3]);
;         const bf16x8 a1 = *(const LAS bf16x8*)(kp + 32 * (DQ * 2) + rd.ko[s & 3]);
;         s0 = MFMA32(a0, qf[s], s0); s1 = MFMA32(a1, qf[s], s1);
;     }
; }
; template <class BiasFn, bool PRE = false>
; DI void at_sm(f32x16& s0, f32x16& s1, f32x16 (&o)[4], float& m, float& l, const float c2, const BiasFn& bias, const int lane, bf16x8 (&pf)[4]) {
;     const int h = lane >> 5;
;     const float nm = -m;
;     int mi = (int)0x80000000;
; #pragma unroll
;     for (int i = 0; i < 16; ++i) {
;         const int key = (i & 3) + 8 * (i >> 2) + 4 * h;
;         if (!PRE) { s0[i] = fmaf(s0[i], c2, bias(key, nm)); s1[i] = fmaf(s1[i], c2, bias(32 + key, nm)); }
;         mi = max(mi, max((int)__float_as_uint(s0[i]), (int)__float_as_uint(s1[i])));
;     }
;     { const auto sw = __builtin_amdgcn_permlane32_swap((unsigned)mi, (unsigned)mi, false, false); mi = max((int)sw[0], (int)sw[1]); }
;     const float mx = __uint_as_float((unsigned)mi);
;     if (__any(mx > 8.0f)) {
;         const float d = fmaxf(mx, 0.f), alpha = __builtin_amdgcn_exp2f(-d);
;         m += d; l *= alpha;
; #pragma unroll
;         for (int t = 0; t < 4; ++t)
; #pragma unroll
;             for (int i = 0; i < 16; ++i) o[t][i] *= alpha;
; #pragma unroll
;         for (int i = 0; i < 16; ++i) { s0[i] -= d; s1[i] -= d; }
;     }
.Lmla_qk2:
	ds_read_b128 v[4:7], v240 offset:49152
	ds_read_b128 v[8:11], v240 offset:49280
	v_xor_b32_e32 v82, 0x80000000, v179
	v_mov_b32_e32 v83, v82
	v_mov_b64_e32 v[84:85], v[82:83]
	v_mov_b64_e32 v[86:87], v[82:83]
	v_mov_b64_e32 v[88:89], v[82:83]
	v_mov_b64_e32 v[90:91], v[82:83]
	v_mov_b64_e32 v[92:93], v[82:83]
	v_mov_b64_e32 v[94:95], v[82:83]
	v_mov_b64_e32 v[96:97], v[82:83]
	s_nop 0
	s_waitcnt lgkmcnt(0)
	v_mfma_f32_32x32x16_bf16 v[98:113], v[4:7], v[158:161], v[82:97]
	ds_read_b128 v[4:7], v240 offset:61440
	ds_read_b128 v[12:15], v240 offset:49408
	s_waitcnt lgkmcnt(0)
	v_mfma_f32_32x32x16_bf16 v[82:97], v[4:7], v[158:161], v[82:97]
	ds_read_b128 v[4:7], v241 offset:49152
	ds_read_b128 v[192:195], v241 offset:49280
	s_waitcnt lgkmcnt(0)
	v_mfma_f32_32x32x16_bf16 v[98:113], v[4:7], v[154:157], v[98:113]
	ds_read_b128 v[4:7], v241 offset:61440
	ds_read_b128 v[196:199], v241 offset:49408
	s_waitcnt lgkmcnt(0)
	v_mfma_f32_32x32x16_bf16 v[82:97], v[4:7], v[154:157], v[82:97]
	ds_read_b128 v[4:7], v242 offset:49152
	ds_read_b128 v[200:203], v242 offset:49280
	s_waitcnt lgkmcnt(0)
	v_mfma_f32_32x32x16_bf16 v[98:113], v[4:7], v[150:153], v[98:113]
	ds_read_b128 v[4:7], v242 offset:61440
	ds_read_b128 v[204:207], v242 offset:49408
	s_waitcnt lgkmcnt(0)
	v_mfma_f32_32x32x16_bf16 v[82:97], v[4:7], v[150:153], v[82:97]
	ds_read_b128 v[4:7], v243 offset:49152
	ds_read_b128 v[208:211], v243 offset:49280
	s_waitcnt lgkmcnt(0)
	v_mfma_f32_32x32x16_bf16 v[98:113], v[4:7], v[146:149], v[98:113]
	ds_read_b128 v[4:7], v243 offset:61440
	ds_read_b128 v[212:215], v243 offset:49408
	s_waitcnt lgkmcnt(0)
	v_mfma_f32_32x32x16_bf16 v[82:97], v[4:7], v[146:149], v[82:97]
	v_mfma_f32_32x32x16_bf16 v[98:113], v[8:11], v[142:145], v[98:113]
	ds_read_b128 v[4:7], v240 offset:61568
	ds_read_b128 v[8:11], v240 offset:61696
	s_waitcnt lgkmcnt(0)
	v_mfma_f32_32x32x16_bf16 v[82:97], v[4:7], v[142:145], v[82:97]
	v_mfma_f32_32x32x16_bf16 v[98:113], v[192:195], v[138:141], v[98:113]
	ds_read_b128 v[4:7], v241 offset:61568
	ds_read_b128 v[192:195], v241 offset:61696
	s_waitcnt lgkmcnt(0)
	v_mfma_f32_32x32x16_bf16 v[82:97], v[4:7], v[138:141], v[82:97]
	v_mfma_f32_32x32x16_bf16 v[98:113], v[200:203], v[134:137], v[98:113]
	ds_read_b128 v[4:7], v242 offset:61568
	ds_read_b128 v[200:203], v242 offset:61696
	s_waitcnt lgkmcnt(0)
	v_mfma_f32_32x32x16_bf16 v[82:97], v[4:7], v[134:137], v[82:97]
	v_mfma_f32_32x32x16_bf16 v[98:113], v[208:211], v[130:133], v[98:113]
	ds_read_b128 v[4:7], v243 offset:61568
	ds_read_b128 v[208:211], v243 offset:61696
	s_waitcnt lgkmcnt(0)
	v_mfma_f32_32x32x16_bf16 v[82:97], v[4:7], v[130:133], v[82:97]
	v_mfma_f32_32x32x16_bf16 v[98:113], v[12:15], v[126:129], v[98:113]
	v_mfma_f32_32x32x16_bf16 v[82:97], v[8:11], v[126:129], v[82:97]
	v_mfma_f32_32x32x16_bf16 v[98:113], v[196:199], v[122:125], v[98:113]
	v_mfma_f32_32x32x16_bf16 v[82:97], v[192:195], v[122:125], v[82:97]
	v_mfma_f32_32x32x16_bf16 v[98:113], v[204:207], v[118:121], v[98:113]
	v_mfma_f32_32x32x16_bf16 v[82:97], v[200:203], v[118:121], v[82:97]
	v_mfma_f32_32x32x16_bf16 v[98:113], v[212:215], v[114:117], v[98:113]
	v_mfma_f32_32x32x16_bf16 v[82:97], v[208:211], v[114:117], v[82:97]
.Lmla_qkd:
	s_nop 11
	v_max3_i32 v4, v82, v83, v84
	v_max3_i32 v5, v85, v86, v87
	v_max3_i32 v6, v88, v89, v90
	v_max3_i32 v7, v91, v92, v93
	v_max3_i32 v8, v94, v95, v96
	v_max3_i32 v9, v97, v98, v99
	v_max3_i32 v10, v100, v101, v102
	v_max3_i32 v11, v103, v104, v105
	v_max3_i32 v12, v106, v107, v108
	v_max3_i32 v13, v109, v110, v111
	v_max3_i32 v4, v4, v5, v6
	v_max3_i32 v5, v7, v8, v9
	v_max3_i32 v6, v10, v11, v12
	v_max3_i32 v7, v13, v112, v113
	v_max3_i32 v2, v4, v5, v6
	v_max_i32_e32 v2, v2, v7
	v_mov_b32_e32 v4, v2
	s_nop 1
	v_permlane32_swap_b32_e32 v2, v4
	v_max_i32_e32 v2, v2, v4
	v_cmp_lt_f32_e32 vcc, s58, v2
	s_cbranch_vccz .LBB0_555
	v_max_f32_e32 v2, v2, v2
	v_max_f32_e32 v4, 0, v2
	v_exp_f32_e64 v2, -v4
	v_add_f32_e32 v179, v179, v4
	v_sub_f32_e32 v113, v113, v4
	v_sub_f32_e32 v112, v112, v4
	v_mul_f32_e32 v173, v173, v2
	v_pk_mul_f32 v[80:81], v[80:81], v[2:3] op_sel_hi:[1,0]
	v_pk_mul_f32 v[78:79], v[78:79], v[2:3] op_sel_hi:[1,0]
	v_pk_mul_f32 v[76:77], v[76:77], v[2:3] op_sel_hi:[1,0]
	v_pk_mul_f32 v[74:75], v[74:75], v[2:3] op_sel_hi:[1,0]
	v_pk_mul_f32 v[72:73], v[72:73], v[2:3] op_sel_hi:[1,0]
	v_pk_mul_f32 v[70:71], v[70:71], v[2:3] op_sel_hi:[1,0]
	v_pk_mul_f32 v[68:69], v[68:69], v[2:3] op_sel_hi:[1,0]
	v_pk_mul_f32 v[66:67], v[66:67], v[2:3] op_sel_hi:[1,0]
	v_pk_mul_f32 v[64:65], v[64:65], v[2:3] op_sel_hi:[1,0]
	v_pk_mul_f32 v[62:63], v[62:63], v[2:3] op_sel_hi:[1,0]
	v_pk_mul_f32 v[60:61], v[60:61], v[2:3] op_sel_hi:[1,0]
	v_pk_mul_f32 v[58:59], v[58:59], v[2:3] op_sel_hi:[1,0]
	v_pk_mul_f32 v[56:57], v[56:57], v[2:3] op_sel_hi:[1,0]
	v_pk_mul_f32 v[54:55], v[54:55], v[2:3] op_sel_hi:[1,0]
	v_pk_mul_f32 v[52:53], v[52:53], v[2:3] op_sel_hi:[1,0]
	v_pk_mul_f32 v[50:51], v[50:51], v[2:3] op_sel_hi:[1,0]
	v_pk_mul_f32 v[48:49], v[48:49], v[2:3] op_sel_hi:[1,0]
	v_pk_mul_f32 v[46:47], v[46:47], v[2:3] op_sel_hi:[1,0]
	v_pk_mul_f32 v[44:45], v[44:45], v[2:3] op_sel_hi:[1,0]
	v_pk_mul_f32 v[42:43], v[42:43], v[2:3] op_sel_hi:[1,0]
	v_pk_mul_f32 v[40:41], v[40:41], v[2:3] op_sel_hi:[1,0]
	v_pk_mul_f32 v[38:39], v[38:39], v[2:3] op_sel_hi:[1,0]
	v_pk_mul_f32 v[36:37], v[36:37], v[2:3] op_sel_hi:[1,0]
	v_pk_mul_f32 v[34:35], v[34:35], v[2:3] op_sel_hi:[1,0]
	v_pk_mul_f32 v[32:33], v[32:33], v[2:3] op_sel_hi:[1,0]
	v_pk_mul_f32 v[30:31], v[30:31], v[2:3] op_sel_hi:[1,0]
	v_pk_mul_f32 v[28:29], v[28:29], v[2:3] op_sel_hi:[1,0]
	v_pk_mul_f32 v[26:27], v[26:27], v[2:3] op_sel_hi:[1,0]
	v_pk_mul_f32 v[24:25], v[24:25], v[2:3] op_sel_hi:[1,0]
	v_pk_mul_f32 v[22:23], v[22:23], v[2:3] op_sel_hi:[1,0]
	v_pk_mul_f32 v[20:21], v[20:21], v[2:3] op_sel_hi:[1,0]
	v_pk_mul_f32 v[18:19], v[18:19], v[2:3] op_sel_hi:[1,0]
	v_sub_f32_e32 v111, v111, v4
	v_sub_f32_e32 v110, v110, v4
	v_sub_f32_e32 v109, v109, v4
	v_sub_f32_e32 v108, v108, v4
	v_sub_f32_e32 v107, v107, v4
	v_sub_f32_e32 v106, v106, v4
	v_sub_f32_e32 v105, v105, v4
	v_sub_f32_e32 v104, v104, v4
	v_sub_f32_e32 v103, v103, v4
	v_sub_f32_e32 v102, v102, v4
	v_sub_f32_e32 v101, v101, v4
	v_sub_f32_e32 v100, v100, v4
	v_sub_f32_e32 v99, v99, v4
	v_sub_f32_e32 v98, v98, v4
	v_sub_f32_e32 v97, v97, v4
	v_sub_f32_e32 v96, v96, v4
	v_sub_f32_e32 v95, v95, v4
	v_sub_f32_e32 v94, v94, v4
	v_sub_f32_e32 v93, v93, v4
	v_sub_f32_e32 v92, v92, v4
	v_sub_f32_e32 v91, v91, v4
	v_sub_f32_e32 v90, v90, v4
	v_sub_f32_e32 v89, v89, v4
	v_sub_f32_e32 v88, v88, v4
	v_sub_f32_e32 v87, v87, v4
	v_sub_f32_e32 v86, v86, v4
	v_sub_f32_e32 v85, v85, v4
	v_sub_f32_e32 v84, v84, v4
	v_sub_f32_e32 v83, v83, v4
	v_sub_f32_e32 v82, v82, v4
	s_branch .LBB0_555
